# DOWN epilogue: dropped the 32 zero-initialising moves of registers whose two fp8 halves are both overwritten before the store
# speedup vs baseline: 1.0057x; 1.0039x over previous
.LBB0_843:
	v_med3_f32 v145, v126, s63, v230
	v_med3_f32 v127, v127, s63, v230
	v_cvt_pk_fp8_f32 v126, v145, v127
	v_med3_f32 v128, v128, s63, v230
	v_med3_f32 v129, v129, s63, v230
	v_med3_f32 v114, v114, s63, v230
	v_cvt_pk_fp8_f32 v126, v128, v129 op_sel:[0,0,1]
	v_med3_f32 v115, v115, s63, v230
	v_cvt_pk_fp8_f32 v129, v114, v115
	v_med3_f32 v115, v117, s63, v230
	v_med3_f32 v117, v110, s63, v230
	v_med3_f32 v111, v111, s63, v230
	v_cvt_pk_fp8_f32 v110, v117, v111
	v_med3_f32 v112, v112, s63, v230
	v_med3_f32 v113, v113, s63, v230
	v_med3_f32 v106, v106, s63, v230
	v_med3_f32 v107, v107, s63, v230
	v_cvt_pk_fp8_f32 v110, v112, v113 op_sel:[0,0,1]
	v_med3_f32 v102, v102, s63, v230
	v_med3_f32 v103, v103, s63, v230
	v_med3_f32 v98, v98, s63, v230
	v_med3_f32 v99, v99, s63, v230
	v_cvt_pk_fp8_f32 v111, v106, v107
	v_cvt_pk_fp8_f32 v112, v102, v103
	v_cvt_pk_fp8_f32 v113, v98, v99
	v_lshl_add_u32 v146, s43, 8, v141
	v_med3_f32 v114, v116, s63, v230
	v_or_b32_e32 v116, 16, v146
	v_med3_f32 v106, v108, s63, v230
	v_med3_f32 v107, v109, s63, v230
	v_med3_f32 v102, v104, s63, v230
	v_med3_f32 v103, v105, s63, v230
	v_med3_f32 v98, v100, s63, v230
	v_med3_f32 v99, v101, s63, v230
	v_cvt_pk_fp8_f32 v111, v106, v107 op_sel:[0,0,1]
	v_cvt_pk_fp8_f32 v112, v102, v103 op_sel:[0,0,1]
	v_cvt_pk_fp8_f32 v113, v98, v99 op_sel:[0,0,1]
	v_ashrrev_i32_e32 v117, 31, v116
	v_lshl_add_u32 v148, s45, 8, v143
	v_lshlrev_b64 v[98:99], 11, v[116:117]
	v_ashrrev_i32_e32 v149, 31, v148
	v_lshl_add_u64 v[98:99], s[10:11], 0, v[98:99]
	v_lshl_add_u64 v[98:99], v[98:99], 0, v[148:149]
	global_store_dwordx4 v[98:99], v[110:113], off
	v_med3_f32 v99, v94, s63, v230
	v_med3_f32 v95, v95, s63, v230
	v_cvt_pk_fp8_f32 v94, v99, v95
	v_med3_f32 v96, v96, s63, v230
	v_med3_f32 v97, v97, s63, v230
	v_med3_f32 v90, v90, s63, v230
	v_med3_f32 v91, v91, s63, v230
	v_cvt_pk_fp8_f32 v94, v96, v97 op_sel:[0,0,1]
	v_med3_f32 v86, v86, s63, v230
	v_med3_f32 v87, v87, s63, v230
	v_med3_f32 v82, v82, s63, v230
	v_med3_f32 v83, v83, s63, v230
	v_cvt_pk_fp8_f32 v95, v90, v91
	v_cvt_pk_fp8_f32 v96, v86, v87
	v_cvt_pk_fp8_f32 v97, v82, v83
	v_or_b32_e32 v98, 32, v146
	v_med3_f32 v90, v92, s63, v230
	v_med3_f32 v91, v93, s63, v230
	v_med3_f32 v86, v88, s63, v230
	v_med3_f32 v87, v89, s63, v230
	v_med3_f32 v82, v84, s63, v230
	v_med3_f32 v83, v85, s63, v230
	v_cvt_pk_fp8_f32 v95, v90, v91 op_sel:[0,0,1]
	v_cvt_pk_fp8_f32 v96, v86, v87 op_sel:[0,0,1]
	v_cvt_pk_fp8_f32 v97, v82, v83 op_sel:[0,0,1]
	v_ashrrev_i32_e32 v99, 31, v98
	v_lshlrev_b64 v[82:83], 11, v[98:99]
	v_lshl_add_u64 v[82:83], s[10:11], 0, v[82:83]
	v_lshl_add_u64 v[82:83], v[82:83], 0, v[148:149]
	global_store_dwordx4 v[82:83], v[94:97], off
	v_med3_f32 v83, v78, s63, v230
	v_med3_f32 v79, v79, s63, v230
	v_cvt_pk_fp8_f32 v78, v83, v79
	v_med3_f32 v80, v80, s63, v230
	v_med3_f32 v81, v81, s63, v230
	v_med3_f32 v74, v74, s63, v230
	v_med3_f32 v75, v75, s63, v230
	v_cvt_pk_fp8_f32 v78, v80, v81 op_sel:[0,0,1]
	v_med3_f32 v70, v70, s63, v230
	v_med3_f32 v71, v71, s63, v230
	v_med3_f32 v66, v66, s63, v230
	v_med3_f32 v67, v67, s63, v230
	v_cvt_pk_fp8_f32 v79, v74, v75
	v_cvt_pk_fp8_f32 v80, v70, v71
	v_cvt_pk_fp8_f32 v81, v66, v67
	v_or_b32_e32 v82, 48, v146
	v_med3_f32 v74, v76, s63, v230
	v_med3_f32 v75, v77, s63, v230
	v_med3_f32 v70, v72, s63, v230
	v_med3_f32 v71, v73, s63, v230
	v_med3_f32 v66, v68, s63, v230
	v_med3_f32 v67, v69, s63, v230
	v_cvt_pk_fp8_f32 v79, v74, v75 op_sel:[0,0,1]
	v_cvt_pk_fp8_f32 v80, v70, v71 op_sel:[0,0,1]
	v_cvt_pk_fp8_f32 v81, v66, v67 op_sel:[0,0,1]
	v_ashrrev_i32_e32 v83, 31, v82
	v_lshlrev_b64 v[66:67], 11, v[82:83]
	v_lshl_add_u64 v[66:67], s[10:11], 0, v[66:67]
	v_lshl_add_u64 v[66:67], v[66:67], 0, v[148:149]
	global_store_dwordx4 v[66:67], v[78:81], off
	v_med3_f32 v66, v62, s63, v230
	v_med3_f32 v63, v63, s63, v230
	v_cvt_pk_fp8_f32 v62, v66, v63
	v_med3_f32 v64, v64, s63, v230
	v_med3_f32 v65, v65, s63, v230
	v_med3_f32 v58, v58, s63, v230
	v_med3_f32 v59, v59, s63, v230
	v_cvt_pk_fp8_f32 v62, v64, v65 op_sel:[0,0,1]
	v_med3_f32 v54, v54, s63, v230
	v_med3_f32 v55, v55, s63, v230
	v_med3_f32 v50, v50, s63, v230
	v_med3_f32 v51, v51, s63, v230
	v_cvt_pk_fp8_f32 v63, v58, v59
	v_cvt_pk_fp8_f32 v64, v54, v55
	v_cvt_pk_fp8_f32 v65, v50, v51
	v_ashrrev_i32_e32 v147, 31, v146
	v_cvt_pk_fp8_f32 v129, v114, v115 op_sel:[0,0,1]
	v_lshlrev_b64 v[114:115], 11, v[146:147]
	v_med3_f32 v58, v60, s63, v230
	v_med3_f32 v59, v61, s63, v230
	v_med3_f32 v54, v56, s63, v230
	v_med3_f32 v55, v57, s63, v230
	v_med3_f32 v50, v52, s63, v230
	v_med3_f32 v51, v53, s63, v230
	v_lshl_add_u64 v[114:115], s[10:11], 0, v[114:115]
	v_cvt_pk_fp8_f32 v63, v58, v59 op_sel:[0,0,1]
	v_cvt_pk_fp8_f32 v64, v54, v55 op_sel:[0,0,1]
	v_cvt_pk_fp8_f32 v65, v50, v51 op_sel:[0,0,1]
	v_lshl_add_u64 v[114:115], v[114:115], 0, v[148:149]
	s_mov_b32 s4, 0x40000
	v_add_co_u32_e32 v50, vcc, s4, v114
	v_med3_f32 v47, v47, s63, v230
	s_nop 0
	v_addc_co_u32_e32 v51, vcc, 0, v115, vcc
	global_store_dwordx4 v[50:51], v[62:65], off
	v_med3_f32 v50, v46, s63, v230
	v_cvt_pk_fp8_f32 v46, v50, v47
	v_med3_f32 v48, v48, s63, v230
	v_med3_f32 v49, v49, s63, v230
	v_med3_f32 v42, v42, s63, v230
	v_med3_f32 v43, v43, s63, v230
	v_cvt_pk_fp8_f32 v46, v48, v49 op_sel:[0,0,1]
	v_med3_f32 v38, v38, s63, v230
	v_med3_f32 v39, v39, s63, v230
	v_med3_f32 v34, v34, s63, v230
	v_med3_f32 v35, v35, s63, v230
	v_cvt_pk_fp8_f32 v47, v42, v43
	v_cvt_pk_fp8_f32 v48, v38, v39
	v_cvt_pk_fp8_f32 v49, v34, v35
	v_med3_f32 v42, v44, s63, v230
	v_med3_f32 v43, v45, s63, v230
	v_med3_f32 v38, v40, s63, v230
	v_med3_f32 v39, v41, s63, v230
	v_med3_f32 v34, v36, s63, v230
	v_med3_f32 v35, v37, s63, v230
	v_cvt_pk_fp8_f32 v47, v42, v43 op_sel:[0,0,1]
	v_cvt_pk_fp8_f32 v48, v38, v39 op_sel:[0,0,1]
	v_cvt_pk_fp8_f32 v49, v34, v35 op_sel:[0,0,1]
	s_mov_b32 s4, 0x48000
	v_add_co_u32_e32 v34, vcc, s4, v114
	v_med3_f32 v31, v31, s63, v230
	s_nop 0
	v_addc_co_u32_e32 v35, vcc, 0, v115, vcc
	global_store_dwordx4 v[34:35], v[46:49], off
	v_med3_f32 v34, v30, s63, v230
	v_cvt_pk_fp8_f32 v30, v34, v31
	v_med3_f32 v32, v32, s63, v230
	v_med3_f32 v33, v33, s63, v230
	v_med3_f32 v26, v26, s63, v230
	v_med3_f32 v27, v27, s63, v230
	v_cvt_pk_fp8_f32 v30, v32, v33 op_sel:[0,0,1]
	v_med3_f32 v22, v22, s63, v230
	v_med3_f32 v23, v23, s63, v230
	v_med3_f32 v18, v18, s63, v230
	v_med3_f32 v19, v19, s63, v230
	v_cvt_pk_fp8_f32 v31, v26, v27
	v_cvt_pk_fp8_f32 v32, v22, v23
	v_cvt_pk_fp8_f32 v33, v18, v19
	v_med3_f32 v26, v28, s63, v230
	v_med3_f32 v27, v29, s63, v230
	v_med3_f32 v22, v24, s63, v230
	v_med3_f32 v23, v25, s63, v230
	v_med3_f32 v18, v20, s63, v230
	v_med3_f32 v19, v21, s63, v230
	v_cvt_pk_fp8_f32 v31, v26, v27 op_sel:[0,0,1]
	v_cvt_pk_fp8_f32 v32, v22, v23 op_sel:[0,0,1]
	v_cvt_pk_fp8_f32 v33, v18, v19 op_sel:[0,0,1]
	s_mov_b32 s4, 0x50000
	v_add_co_u32_e32 v18, vcc, s4, v114
	v_med3_f32 v15, v15, s63, v230
	s_nop 0
	v_addc_co_u32_e32 v19, vcc, 0, v115, vcc
	global_store_dwordx4 v[18:19], v[30:33], off
	v_med3_f32 v18, v14, s63, v230
	v_cvt_pk_fp8_f32 v14, v18, v15
	v_med3_f32 v16, v16, s63, v230
	v_med3_f32 v17, v17, s63, v230
	v_med3_f32 v122, v122, s63, v230
	v_med3_f32 v123, v123, s63, v230
	v_med3_f32 v118, v118, s63, v230
	v_med3_f32 v119, v119, s63, v230
	v_med3_f32 v10, v10, s63, v230
	v_med3_f32 v11, v11, s63, v230
	v_cvt_pk_fp8_f32 v14, v16, v17 op_sel:[0,0,1]
	v_med3_f32 v6, v6, s63, v230
	v_med3_f32 v7, v7, s63, v230
	v_med3_f32 v2, v2, s63, v230
	v_med3_f32 v3, v3, s63, v230
	v_cvt_pk_fp8_f32 v127, v122, v123
	v_cvt_pk_fp8_f32 v128, v118, v119
	v_cvt_pk_fp8_f32 v15, v10, v11
	v_cvt_pk_fp8_f32 v16, v6, v7
	v_cvt_pk_fp8_f32 v17, v2, v3
	v_med3_f32 v122, v124, s63, v230
	v_med3_f32 v123, v125, s63, v230
	v_med3_f32 v118, v120, s63, v230
	v_med3_f32 v119, v121, s63, v230
	v_med3_f32 v10, v12, s63, v230
	v_med3_f32 v11, v13, s63, v230
	v_med3_f32 v6, v8, s63, v230
	v_med3_f32 v7, v9, s63, v230
	v_med3_f32 v2, v4, s63, v230
	v_med3_f32 v3, v5, s63, v230
	v_cvt_pk_fp8_f32 v127, v122, v123 op_sel:[0,0,1]
	v_cvt_pk_fp8_f32 v128, v118, v119 op_sel:[0,0,1]
	v_cvt_pk_fp8_f32 v15, v10, v11 op_sel:[0,0,1]
	v_cvt_pk_fp8_f32 v16, v6, v7 op_sel:[0,0,1]
	v_cvt_pk_fp8_f32 v17, v2, v3 op_sel:[0,0,1]
	v_add_co_u32_e32 v2, vcc, 0x58000, v114
	s_mov_b64 s[4:5], -1
	s_nop 0
	v_addc_co_u32_e32 v3, vcc, 0, v115, vcc
	s_andn2_b64 vcc, exec, s[6:7]
	global_store_dwordx4 v[114:115], v[126:129], off
	global_store_dwordx4 v[2:3], v[14:17], off
	s_cbranch_vccnz .LBB0_835
	s_andn2_b64 vcc, exec, s[12:13]
	s_cbranch_vccnz .LBB0_834
	s_barrier
	s_branch .LBB0_834
